# priority raise for unit-1 waves plus the two units one barrier apart
# baseline (speedup 1.0000x reference)
.LBB0_427:
	v_or_b32_e32 v3, s3, v7
	v_lshlrev_b32_e32 v3, s1, v3
	v_add_u32_e32 v180, s42, v3
	s_movk_i32 s4, 0x1880
	v_mov_b64_e32 v[10:11], s[84:85]
	v_mad_i64_i32 v[10:11], s[4:5], v180, s4, v[10:11]
	s_lshl_b32 s4, s2, 1
	s_mov_b32 s5, 0
	v_lshl_add_u64 v[10:11], v[10:11], 0, s[4:5]
	v_lshlrev_b32_e32 v12, 4, v6
	v_mov_b32_e32 v13, 0
	v_lshl_add_u64 v[10:11], v[10:11], 0, v[12:13]
	global_load_dwordx4 v[146:149], v[10:11], off offset:96
	global_load_dwordx4 v[150:153], v[10:11], off offset:64
	global_load_dwordx4 v[154:157], v[10:11], off offset:32
	global_load_dwordx4 v[158:161], v[10:11], off
	s_lshl_b32 s81, 1, s1
	s_lshl_b32 s1, 0xffffff80, s1
	s_waitcnt vmcnt(0)
	s_add_i32 s82, s42, s1
	v_lshlrev_b32_e32 v2, 4, v2
	s_movk_i32 s1, 0x1000
	v_add3_u32 v182, v1, v2, s1
	s_movk_i32 s16, 0x1880
	v_and_b32_e32 v100, 63, v0
	v_lshrrev_b32_e32 v101, 3, v100
	v_and_b32_e32 v104, 7, v100
	v_xor_b32_e32 v104, v104, v101
	v_lshlrev_b32_e32 v104, 4, v104
	s_lshl_b32 s10, s88, 7
	s_add_u32 s10, s10, 0x800
	v_add_u32_e32 v104, s10, v104
	s_bfe_u32 s11, s75, 0x2000c
	s_and_b32 s12, s75, 0xffff0000
	s_add_u32 s12, s12, 0x8000
	s_add_u32 s13, s11, 1
	s_lshl_b32 s10, s13, 5
	v_add_u32_e32 v102, s10, v101
	v_mul_u32_u24_e32 v103, s81, v102
	v_add_u32_e32 v103, s82, v103
	s_lshl_b32 s10, s13, 12
	s_add_u32 s10, s10, s12
	s_lshl_b32 s13, s81, 3
	v_max_i32_e32 v106, 0, v103
	s_mov_b32 m0, s10
	v_mad_u32_u24 v108, v106, s16, v104
	global_load_lds_dwordx4 v108, s[84:85]
	v_add_u32_e32 v103, s13, v103
	v_max_i32_e32 v106, 0, v103
	s_add_u32 m0, s10, 0x400
	v_mad_u32_u24 v108, v106, s16, v104
	global_load_lds_dwordx4 v108, s[84:85]
	v_add_u32_e32 v103, s13, v103
	v_max_i32_e32 v106, 0, v103
	s_add_u32 m0, s10, 0x800
	v_mad_u32_u24 v108, v106, s16, v104
	global_load_lds_dwordx4 v108, s[84:85]
	v_add_u32_e32 v103, s13, v103
	v_max_i32_e32 v106, 0, v103
	s_add_u32 m0, s10, 0xc00
	v_mad_u32_u24 v108, v106, s16, v104
	global_load_lds_dwordx4 v108, s[84:85]
	s_add_u32 s13, s11, 4
	s_cmp_eq_u32 s11, 0
	s_cselect_b32 s13, 0, s13
	s_lshl_b32 s10, s13, 5
	v_add_u32_e32 v102, s10, v101
	v_mul_u32_u24_e32 v103, s81, v102
	v_add_u32_e32 v103, s82, v103
	s_lshl_b32 s10, s13, 12
	s_add_u32 s10, s10, s12
	s_lshl_b32 s13, s81, 3
	v_max_i32_e32 v106, 0, v103
	s_mov_b32 m0, s10
	v_mad_u32_u24 v108, v106, s16, v104
	global_load_lds_dwordx4 v108, s[84:85]
	v_add_u32_e32 v103, s13, v103
	v_max_i32_e32 v106, 0, v103
	s_add_u32 m0, s10, 0x400
	v_mad_u32_u24 v108, v106, s16, v104
	global_load_lds_dwordx4 v108, s[84:85]
	v_add_u32_e32 v103, s13, v103
	v_max_i32_e32 v106, 0, v103
	s_add_u32 m0, s10, 0x800
	v_mad_u32_u24 v108, v106, s16, v104
	global_load_lds_dwordx4 v108, s[84:85]
	v_add_u32_e32 v103, s13, v103
	v_max_i32_e32 v106, 0, v103
	s_add_u32 m0, s10, 0xc00
	v_mad_u32_u24 v108, v106, s16, v104
	global_load_lds_dwordx4 v108, s[84:85]
	v_and_b32_e32 v100, 63, v0
	v_lshrrev_b32_e32 v101, 3, v100
	v_and_b32_e32 v104, 7, v100
	v_xor_b32_e32 v104, v104, v101
	v_lshlrev_b32_e32 v104, 4, v104
	s_lshl_b32 s10, s88, 7
	s_add_u32 s10, s10, 0x1000
	v_add_u32_e32 v104, s10, v104
	s_bfe_u32 s11, s75, 0x2000c
	s_and_b32 s12, s75, 0xffff0000
	s_add_u32 s13, s11, 1
	s_lshl_b32 s10, s13, 5
	v_add_u32_e32 v102, s10, v101
	v_mul_u32_u24_e32 v103, s81, v102
	v_add_u32_e32 v103, s82, v103
	s_lshl_b32 s10, s13, 12
	s_add_u32 s10, s10, s12
	s_lshl_b32 s13, s81, 3
	v_max_i32_e32 v106, 0, v103
	s_mov_b32 m0, s10
	v_mad_u32_u24 v108, v106, s16, v104
	global_load_lds_dwordx4 v108, s[84:85]
	v_add_u32_e32 v103, s13, v103
	v_max_i32_e32 v106, 0, v103
	s_add_u32 m0, s10, 0x400
	v_mad_u32_u24 v108, v106, s16, v104
	global_load_lds_dwordx4 v108, s[84:85]
	v_add_u32_e32 v103, s13, v103
	v_max_i32_e32 v106, 0, v103
	s_add_u32 m0, s10, 0x800
	v_mad_u32_u24 v108, v106, s16, v104
	global_load_lds_dwordx4 v108, s[84:85]
	v_add_u32_e32 v103, s13, v103
	v_max_i32_e32 v106, 0, v103
	s_add_u32 m0, s10, 0xc00
	v_mad_u32_u24 v108, v106, s16, v104
	global_load_lds_dwordx4 v108, s[84:85]
	s_add_u32 s13, s11, 4
	s_cmp_eq_u32 s11, 0
	s_cselect_b32 s13, 0, s13
	s_lshl_b32 s10, s13, 5
	v_add_u32_e32 v102, s10, v101
	v_mul_u32_u24_e32 v103, s81, v102
	v_add_u32_e32 v103, s82, v103
	s_lshl_b32 s10, s13, 12
	s_add_u32 s10, s10, s12
	s_lshl_b32 s13, s81, 3
	v_max_i32_e32 v106, 0, v103
	s_mov_b32 m0, s10
	v_mad_u32_u24 v108, v106, s16, v104
	global_load_lds_dwordx4 v108, s[84:85]
	v_add_u32_e32 v103, s13, v103
	v_max_i32_e32 v106, 0, v103
	s_add_u32 m0, s10, 0x400
	v_mad_u32_u24 v108, v106, s16, v104
	global_load_lds_dwordx4 v108, s[84:85]
	v_add_u32_e32 v103, s13, v103
	v_max_i32_e32 v106, 0, v103
	s_add_u32 m0, s10, 0x800
	v_mad_u32_u24 v108, v106, s16, v104
	global_load_lds_dwordx4 v108, s[84:85]
	v_add_u32_e32 v103, s13, v103
	v_max_i32_e32 v106, 0, v103
	s_add_u32 m0, s10, 0xc00
	v_mad_u32_u24 v108, v106, s16, v104
	global_load_lds_dwordx4 v108, s[84:85]
	s_waitcnt vmcnt(0)
	s_barrier
	v_readlane_b32 s10, v254, 14
	s_cmp_eq_u32 s10, 0
	s_cbranch_scc1 .Latt_off0
	s_barrier
